# v92: v91 + the 29 in-place add-zero instructions of the M3 pooling window sums deleted
# speedup vs baseline: 1.0070x; 1.0008x over previous
.LBB0_599:
	v_add_u32_e32 v1, s26, v114
	v_add_u32_e32 v105, 1, v1
	v_max_i32_e32 v106, 1, v1
	v_min_i32_e32 v105, s14, v105
	v_sub_u32_e32 v105, v105, v106
	v_add_u32_e32 v105, 1, v105
	v_cvt_f32_i32_e32 v105, v105
	ds_read_b128 v[72:75], v124 offset:3696
	ds_read_b128 v[76:79], v124 offset:4224
	v_div_scale_f32 v107, s[10:11], v105, v105, 1.0
	v_rcp_f32_e32 v141, v107
	s_waitcnt lgkmcnt(1)
	v_lshlrev_b32_e32 v2, 16, v72
	v_and_b32_e32 v3, 0xffff0000, v72
	v_lshlrev_b32_e32 v72, 16, v73
	v_fma_f32 v142, -v107, v141, 1.0
	v_fmac_f32_e32 v141, v142, v141
	v_div_scale_f32 v142, vcc, 1.0, v105, 1.0
	v_mul_f32_e32 v143, v142, v141
	v_fma_f32 v144, -v107, v143, v142
	v_fmac_f32_e32 v143, v144, v141
	v_and_b32_e32 v73, 0xffff0000, v73
	v_lshlrev_b32_e32 v80, 16, v74
	v_and_b32_e32 v74, 0xffff0000, v74
	v_lshlrev_b32_e32 v81, 16, v75
	v_and_b32_e32 v75, 0xffff0000, v75
	v_fma_f32 v107, -v107, v143, v142
	s_waitcnt lgkmcnt(0)
	v_lshlrev_b32_e32 v101, 16, v76
	v_and_b32_e32 v76, 0xffff0000, v76
	v_lshlrev_b32_e32 v103, 16, v77
	v_and_b32_e32 v77, 0xffff0000, v77
	v_lshlrev_b32_e32 v104, 16, v78
	v_and_b32_e32 v78, 0xffff0000, v78
	v_lshlrev_b32_e32 v106, 16, v79
	v_and_b32_e32 v79, 0xffff0000, v79
	v_div_fmas_f32 v107, v107, v141, v143
	v_add_f32_e32 v3, v3, v76
	v_add_f32_e32 v72, v72, v103
	v_add_f32_e32 v73, v73, v77
	v_add_f32_e32 v80, v80, v104
	v_add_f32_e32 v74, v74, v78
	v_add_f32_e32 v81, v81, v106
	v_add_f32_e32 v75, v75, v79
	v_div_fixup_f32 v105, v107, v105, 1.0
	v_add_f32_e32 v2, v2, v101
	v_fma_f32 v3, v105, v3, -v76
	v_fma_f32 v76, v105, v72, -v103
	v_fma_f32 v73, v105, v73, -v77
	v_fma_f32 v77, v105, v80, -v104
	v_fma_f32 v74, v105, v74, -v78
	v_fma_f32 v78, v105, v81, -v106
	v_fma_f32 v75, v105, v75, -v79
	v_fma_f32 v2, v105, v2, -v101
	v_cvt_pk_bf16_f32 v72, v2, v3
	v_cvt_pk_bf16_f32 v73, v76, v73
	v_cvt_pk_bf16_f32 v74, v77, v74
	v_cvt_pk_bf16_f32 v75, v78, v75
	ds_read_b128 v[76:79], v124 offset:3296
	ds_write_b128 v124, v[72:75] offset:45056
	ds_read_b128 v[72:75], v124 offset:3824
	s_waitcnt lgkmcnt(2)
	v_and_b32_e32 v3, 0xffff0000, v76
	v_lshlrev_b32_e32 v81, 16, v79
	v_and_b32_e32 v79, 0xffff0000, v79
	v_lshlrev_b32_e32 v2, 16, v76
	v_lshlrev_b32_e32 v76, 16, v77
	v_add_f32_e32 v101, 0, v79
	s_waitcnt lgkmcnt(0)
	v_lshlrev_b32_e32 v79, 16, v72
	v_and_b32_e32 v72, 0xffff0000, v72
	v_and_b32_e32 v77, 0xffff0000, v77
	v_add_f32_e32 v3, v3, v72
	v_lshlrev_b32_e32 v72, 16, v73
	v_lshlrev_b32_e32 v80, 16, v78
	v_add_f32_e32 v103, v76, v72
	v_and_b32_e32 v72, 0xffff0000, v73
	v_and_b32_e32 v78, 0xffff0000, v78
	v_add_f32_e32 v104, v77, v72
	v_lshlrev_b32_e32 v72, 16, v74
	v_add_f32_e32 v80, v80, v72
	v_and_b32_e32 v72, 0xffff0000, v74
	v_add_f32_e32 v105, v78, v72
	v_lshlrev_b32_e32 v72, 16, v75
	v_add_f32_e32 v2, v2, v79
	ds_read_b128 v[76:79], v124 offset:4352
	v_add_f32_e32 v81, v81, v72
	v_and_b32_e32 v72, 0xffff0000, v75
	v_add_f32_e32 v101, v101, v72
	ds_read_b128 v[72:75], v124 offset:4880
	s_waitcnt lgkmcnt(1)
	v_lshlrev_b32_e32 v106, 16, v76
	v_and_b32_e32 v76, 0xffff0000, v76
	v_add_f32_e32 v3, v3, v76
	v_lshlrev_b32_e32 v107, 16, v77
	s_waitcnt lgkmcnt(0)
	v_lshlrev_b32_e32 v143, 16, v72
	v_and_b32_e32 v72, 0xffff0000, v72
	v_add_f32_e32 v103, v103, v107
	v_lshlrev_b32_e32 v141, 16, v78
	v_add_f32_e32 v3, v3, v72
	v_lshlrev_b32_e32 v72, 16, v73
	v_and_b32_e32 v77, 0xffff0000, v77
	v_add_f32_e32 v80, v80, v141
	v_add_f32_e32 v72, v103, v72
	v_lshlrev_b32_e32 v103, 16, v74
	v_add_f32_e32 v104, v104, v77
	v_and_b32_e32 v73, 0xffff0000, v73
	v_add_f32_e32 v80, v80, v103
	v_add_u32_e32 v103, 2, v1
	v_add_f32_e32 v73, v104, v73
	v_max_i32_e32 v104, 2, v1
	v_min_i32_e32 v103, s14, v103
	v_sub_u32_e32 v103, v103, v104
	v_add_u32_e32 v103, 2, v103
	v_cvt_f32_i32_e32 v103, v103
	v_and_b32_e32 v78, 0xffff0000, v78
	v_add_f32_e32 v105, v105, v78
	v_and_b32_e32 v74, 0xffff0000, v74
	v_add_f32_e32 v2, v2, v106
	v_add_f32_e32 v74, v105, v74
	v_div_scale_f32 v105, s[10:11], v103, v103, 1.0
	v_add_f32_e32 v2, v2, v143
	v_rcp_f32_e32 v143, v105
	v_lshlrev_b32_e32 v142, 16, v79
	v_and_b32_e32 v79, 0xffff0000, v79
	v_add_f32_e32 v101, v101, v79
	v_lshlrev_b32_e32 v104, 16, v75
	v_and_b32_e32 v75, 0xffff0000, v75
	v_add_f32_e32 v75, v101, v75
	v_fma_f32 v101, -v105, v143, 1.0
	v_add_f32_e32 v81, v81, v142
	v_fmac_f32_e32 v143, v101, v143
	v_div_scale_f32 v101, vcc, 1.0, v103, 1.0
	v_add_f32_e32 v81, v81, v104
	v_mul_f32_e32 v104, v101, v143
	v_fma_f32 v144, -v105, v104, v101
	v_fmac_f32_e32 v104, v144, v143
	v_fma_f32 v101, -v105, v104, v101
	v_div_fmas_f32 v101, v101, v143, v104
	v_div_fixup_f32 v101, v101, v103, 1.0
	v_fma_f32 v3, v101, v3, -v76
	v_fma_f32 v76, v101, v72, -v107
	v_fma_f32 v73, v101, v73, -v77
	v_fma_f32 v77, v101, v80, -v141
	v_fma_f32 v74, v101, v74, -v78
	v_fma_f32 v78, v101, v81, -v142
	v_fma_f32 v75, v101, v75, -v79
	v_fma_f32 v2, v101, v2, -v106
	v_cvt_pk_bf16_f32 v72, v2, v3
	v_cvt_pk_bf16_f32 v73, v76, v73
	v_cvt_pk_bf16_f32 v74, v77, v74
	v_cvt_pk_bf16_f32 v75, v78, v75
	ds_read_b128 v[76:79], v124 offset:2368
	ds_write_b128 v124, v[72:75] offset:45184
	ds_read_b128 v[72:75], v124 offset:2896
	s_waitcnt lgkmcnt(2)
	v_and_b32_e32 v3, 0xffff0000, v76
	v_lshlrev_b32_e32 v81, 16, v79
	v_and_b32_e32 v79, 0xffff0000, v79
	v_lshlrev_b32_e32 v2, 16, v76
	v_lshlrev_b32_e32 v76, 16, v77
	v_add_f32_e32 v101, 0, v79
	s_waitcnt lgkmcnt(0)
	v_lshlrev_b32_e32 v79, 16, v72
	v_and_b32_e32 v72, 0xffff0000, v72
	v_and_b32_e32 v77, 0xffff0000, v77
	v_add_f32_e32 v3, v3, v72
	v_lshlrev_b32_e32 v72, 16, v73
	v_lshlrev_b32_e32 v80, 16, v78
	v_add_f32_e32 v103, v76, v72
	v_and_b32_e32 v72, 0xffff0000, v73
	v_and_b32_e32 v78, 0xffff0000, v78
	v_add_f32_e32 v104, v77, v72
	v_lshlrev_b32_e32 v72, 16, v74
	v_add_f32_e32 v80, v80, v72
	v_and_b32_e32 v72, 0xffff0000, v74
	v_add_f32_e32 v2, v2, v79
	v_add_f32_e32 v105, v78, v72
	ds_read_b128 v[76:79], v124 offset:3424
	v_lshlrev_b32_e32 v72, 16, v75
	v_add_f32_e32 v81, v81, v72
	v_and_b32_e32 v72, 0xffff0000, v75
	v_add_f32_e32 v101, v101, v72
	ds_read_b128 v[72:75], v124 offset:3952
	s_waitcnt lgkmcnt(1)
	v_lshlrev_b32_e32 v106, 16, v76
	v_and_b32_e32 v76, 0xffff0000, v76
	v_add_f32_e32 v3, v3, v76
	v_lshlrev_b32_e32 v76, 16, v77
	v_add_f32_e32 v76, v103, v76
	v_lshlrev_b32_e32 v103, 16, v78
	v_add_f32_e32 v80, v80, v103
	v_lshlrev_b32_e32 v103, 16, v79
	v_and_b32_e32 v79, 0xffff0000, v79
	v_add_f32_e32 v101, v101, v79
	s_waitcnt lgkmcnt(0)
	v_lshlrev_b32_e32 v79, 16, v72
	v_and_b32_e32 v72, 0xffff0000, v72
	v_and_b32_e32 v77, 0xffff0000, v77
	v_add_f32_e32 v3, v3, v72
	v_lshlrev_b32_e32 v72, 16, v73
	v_add_f32_e32 v77, v104, v77
	v_add_f32_e32 v81, v81, v103
	v_add_f32_e32 v103, v76, v72
	v_and_b32_e32 v72, 0xffff0000, v73
	v_and_b32_e32 v78, 0xffff0000, v78
	v_add_f32_e32 v104, v77, v72
	v_lshlrev_b32_e32 v72, 16, v74
	v_add_f32_e32 v2, v2, v106
	v_add_f32_e32 v78, v105, v78
	v_add_f32_e32 v80, v80, v72
	v_and_b32_e32 v72, 0xffff0000, v74
	v_add_f32_e32 v2, v2, v79
	v_add_f32_e32 v105, v78, v72
	v_lshlrev_b32_e32 v72, 16, v75
	ds_read_b128 v[76:79], v124 offset:4480
	v_add_f32_e32 v81, v81, v72
	v_and_b32_e32 v72, 0xffff0000, v75
	v_add_f32_e32 v101, v101, v72
	ds_read_b128 v[72:75], v124 offset:5008
	s_waitcnt lgkmcnt(1)
	v_lshlrev_b32_e32 v141, 16, v77
	v_lshlrev_b32_e32 v106, 16, v76
	v_and_b32_e32 v107, 0xffff0000, v76
	v_add_f32_e32 v76, v103, v141
	v_and_b32_e32 v103, 0xffff0000, v77
	v_and_b32_e32 v142, 0xffff0000, v78
	v_add_f32_e32 v3, v3, v107
	v_add_f32_e32 v77, v104, v103
	v_lshlrev_b32_e32 v104, 16, v78
	v_add_f32_e32 v78, v105, v142
	v_lshlrev_b32_e32 v105, 16, v79
	v_and_b32_e32 v143, 0xffff0000, v79
	s_waitcnt lgkmcnt(0)
	v_lshlrev_b32_e32 v79, 16, v72
	v_and_b32_e32 v72, 0xffff0000, v72
	v_add_f32_e32 v3, v3, v72
	v_lshlrev_b32_e32 v72, 16, v73
	v_add_f32_e32 v144, v76, v72
	v_and_b32_e32 v72, 0xffff0000, v73
	v_add_f32_e32 v80, v80, v104
	v_add_f32_e32 v145, v77, v72
	v_lshlrev_b32_e32 v72, 16, v74
	v_add_f32_e32 v2, v2, v106
	v_add_f32_e32 v80, v80, v72
	v_and_b32_e32 v72, 0xffff0000, v74
	v_add_f32_e32 v2, v2, v79
	v_add_f32_e32 v146, v78, v72
	ds_read_b128 v[76:79], v124 offset:5536
	v_add_f32_e32 v81, v81, v105
	v_lshlrev_b32_e32 v72, 16, v75
	v_add_f32_e32 v101, v101, v143
	v_add_f32_e32 v81, v81, v72
	v_and_b32_e32 v72, 0xffff0000, v75
	v_add_f32_e32 v101, v101, v72
	ds_read_b128 v[72:75], v124 offset:6064
	s_waitcnt lgkmcnt(1)
	v_lshlrev_b32_e32 v147, 16, v76
	v_and_b32_e32 v76, 0xffff0000, v76
	v_add_f32_e32 v3, v3, v76
	v_lshlrev_b32_e32 v76, 16, v77
	v_add_f32_e32 v76, v144, v76
	v_lshlrev_b32_e32 v144, 16, v78
	v_add_f32_e32 v80, v80, v144
	v_lshlrev_b32_e32 v144, 16, v79
	v_and_b32_e32 v79, 0xffff0000, v79
	v_and_b32_e32 v77, 0xffff0000, v77
	v_add_f32_e32 v79, v101, v79
	s_waitcnt lgkmcnt(0)
	v_lshlrev_b32_e32 v101, 16, v72
	v_and_b32_e32 v72, 0xffff0000, v72
	v_add_f32_e32 v77, v145, v77
	v_add_f32_e32 v3, v3, v72
	v_lshlrev_b32_e32 v72, 16, v73
	v_and_b32_e32 v73, 0xffff0000, v73
	v_add_f32_e32 v72, v76, v72
	v_add_f32_e32 v73, v77, v73
	v_lshlrev_b32_e32 v76, 16, v74
	v_add_u32_e32 v77, 4, v1
	v_add_f32_e32 v76, v80, v76
	v_max_i32_e32 v80, 4, v1
	v_min_i32_e32 v77, s14, v77
	v_sub_u32_e32 v77, v77, v80
	v_add_u32_e32 v77, 4, v77
	v_cvt_f32_i32_e32 v77, v77
	v_add_f32_e32 v2, v2, v147
	v_add_f32_e32 v2, v2, v101
	v_and_b32_e32 v78, 0xffff0000, v78
	v_div_scale_f32 v80, s[10:11], v77, v77, 1.0
	v_rcp_f32_e32 v101, v80
	v_add_f32_e32 v78, v146, v78
	v_and_b32_e32 v74, 0xffff0000, v74
	v_add_f32_e32 v74, v78, v74
	v_lshlrev_b32_e32 v78, 16, v75
	v_and_b32_e32 v75, 0xffff0000, v75
	v_add_f32_e32 v75, v79, v75
	v_fma_f32 v79, -v80, v101, 1.0
	v_add_f32_e32 v81, v81, v144
	v_fmac_f32_e32 v101, v79, v101
	v_div_scale_f32 v79, vcc, 1.0, v77, 1.0
	v_add_f32_e32 v78, v81, v78
	v_mul_f32_e32 v81, v79, v101
	v_fma_f32 v144, -v80, v81, v79
	v_fmac_f32_e32 v81, v144, v101
	v_fma_f32 v79, -v80, v81, v79
	v_div_fmas_f32 v79, v79, v101, v81
	v_div_fixup_f32 v77, v79, v77, 1.0
	v_fma_f32 v79, v77, v72, -v141
	v_fma_f32 v73, v77, v73, -v103
	v_fma_f32 v76, v77, v76, -v104
	v_fma_f32 v74, v77, v74, -v142
	v_fma_f32 v78, v77, v78, -v105
	v_fma_f32 v75, v77, v75, -v143
	v_fma_f32 v2, v77, v2, -v106
	v_fma_f32 v3, v77, v3, -v107
	v_cvt_pk_bf16_f32 v72, v2, v3
	v_cvt_pk_bf16_f32 v73, v79, v73
	v_cvt_pk_bf16_f32 v74, v76, v74
	v_cvt_pk_bf16_f32 v75, v78, v75
	ds_read_b128 v[76:79], v124 offset:384
	ds_write_b128 v124, v[72:75] offset:45312
	ds_read_b128 v[72:75], v124 offset:912
	s_waitcnt lgkmcnt(2)
	v_and_b32_e32 v3, 0xffff0000, v76
	v_lshlrev_b32_e32 v81, 16, v79
	v_and_b32_e32 v79, 0xffff0000, v79
	v_lshlrev_b32_e32 v2, 16, v76
	v_lshlrev_b32_e32 v76, 16, v77
	v_add_f32_e32 v101, 0, v79
	s_waitcnt lgkmcnt(0)
	v_lshlrev_b32_e32 v79, 16, v72
	v_and_b32_e32 v72, 0xffff0000, v72
	v_and_b32_e32 v77, 0xffff0000, v77
	v_add_f32_e32 v3, v3, v72
	v_lshlrev_b32_e32 v72, 16, v73
	v_lshlrev_b32_e32 v80, 16, v78
	v_add_f32_e32 v103, v76, v72
	v_and_b32_e32 v72, 0xffff0000, v73
	v_and_b32_e32 v78, 0xffff0000, v78
	v_add_f32_e32 v104, v77, v72
	v_lshlrev_b32_e32 v72, 16, v74
	v_add_f32_e32 v80, v80, v72
	v_and_b32_e32 v72, 0xffff0000, v74
	v_add_f32_e32 v2, v2, v79
	v_add_f32_e32 v105, v78, v72
	ds_read_b128 v[76:79], v124 offset:1440
	v_lshlrev_b32_e32 v72, 16, v75
	v_add_f32_e32 v81, v81, v72
	v_and_b32_e32 v72, 0xffff0000, v75
	v_add_f32_e32 v101, v101, v72
	ds_read_b128 v[72:75], v124 offset:1968
	s_waitcnt lgkmcnt(1)
	v_lshlrev_b32_e32 v106, 16, v76
	v_and_b32_e32 v76, 0xffff0000, v76
	v_add_f32_e32 v3, v3, v76
	v_lshlrev_b32_e32 v76, 16, v77
	v_add_f32_e32 v76, v103, v76
	v_lshlrev_b32_e32 v103, 16, v78
	v_add_f32_e32 v80, v80, v103
	v_lshlrev_b32_e32 v103, 16, v79
	v_and_b32_e32 v79, 0xffff0000, v79
	v_add_f32_e32 v101, v101, v79
	s_waitcnt lgkmcnt(0)
	v_lshlrev_b32_e32 v79, 16, v72
	v_and_b32_e32 v72, 0xffff0000, v72
	v_and_b32_e32 v77, 0xffff0000, v77
	v_add_f32_e32 v3, v3, v72
	v_lshlrev_b32_e32 v72, 16, v73
	v_add_f32_e32 v77, v104, v77
	v_add_f32_e32 v81, v81, v103
	v_add_f32_e32 v103, v76, v72
	v_and_b32_e32 v72, 0xffff0000, v73
	v_and_b32_e32 v78, 0xffff0000, v78
	v_add_f32_e32 v104, v77, v72
	v_lshlrev_b32_e32 v72, 16, v74
	v_add_f32_e32 v2, v2, v106
	v_add_f32_e32 v78, v105, v78
	v_add_f32_e32 v80, v80, v72
	v_and_b32_e32 v72, 0xffff0000, v74
	v_add_f32_e32 v2, v2, v79
	v_add_f32_e32 v105, v78, v72
	ds_read_b128 v[76:79], v124 offset:2496
	v_lshlrev_b32_e32 v72, 16, v75
	v_add_f32_e32 v81, v81, v72
	v_and_b32_e32 v72, 0xffff0000, v75
	v_add_f32_e32 v101, v101, v72
	ds_read_b128 v[72:75], v124 offset:3024
	s_waitcnt lgkmcnt(1)
	v_lshlrev_b32_e32 v106, 16, v76
	v_and_b32_e32 v76, 0xffff0000, v76
	v_add_f32_e32 v3, v3, v76
	v_lshlrev_b32_e32 v76, 16, v77
	v_add_f32_e32 v76, v103, v76
	v_lshlrev_b32_e32 v103, 16, v78
	v_add_f32_e32 v80, v80, v103
	v_lshlrev_b32_e32 v103, 16, v79
	v_and_b32_e32 v79, 0xffff0000, v79
	v_add_f32_e32 v101, v101, v79
	s_waitcnt lgkmcnt(0)
	v_lshlrev_b32_e32 v79, 16, v72
	v_and_b32_e32 v72, 0xffff0000, v72
	v_and_b32_e32 v77, 0xffff0000, v77
	v_add_f32_e32 v3, v3, v72
	v_lshlrev_b32_e32 v72, 16, v73
	v_add_f32_e32 v77, v104, v77
	v_add_f32_e32 v81, v81, v103
	v_add_f32_e32 v103, v76, v72
	v_and_b32_e32 v72, 0xffff0000, v73
	v_and_b32_e32 v78, 0xffff0000, v78
	v_add_f32_e32 v104, v77, v72
	v_lshlrev_b32_e32 v72, 16, v74
	v_add_f32_e32 v2, v2, v106
	v_add_f32_e32 v78, v105, v78
	v_add_f32_e32 v80, v80, v72
	v_and_b32_e32 v72, 0xffff0000, v74
	v_add_f32_e32 v2, v2, v79
	v_add_f32_e32 v105, v78, v72
	ds_read_b128 v[76:79], v124 offset:3552
	v_lshlrev_b32_e32 v72, 16, v75
	v_add_f32_e32 v81, v81, v72
	v_and_b32_e32 v72, 0xffff0000, v75
	v_add_f32_e32 v101, v101, v72
	ds_read_b128 v[72:75], v124 offset:4080
	s_waitcnt lgkmcnt(1)
	v_lshlrev_b32_e32 v106, 16, v76
	v_and_b32_e32 v76, 0xffff0000, v76
	v_add_f32_e32 v3, v3, v76
	v_lshlrev_b32_e32 v76, 16, v77
	v_add_f32_e32 v76, v103, v76
	v_lshlrev_b32_e32 v103, 16, v78
	v_add_f32_e32 v80, v80, v103
	v_lshlrev_b32_e32 v103, 16, v79
	v_and_b32_e32 v79, 0xffff0000, v79
	v_add_f32_e32 v101, v101, v79
	s_waitcnt lgkmcnt(0)
	v_lshlrev_b32_e32 v79, 16, v72
	v_and_b32_e32 v72, 0xffff0000, v72
	v_and_b32_e32 v77, 0xffff0000, v77
	v_add_f32_e32 v3, v3, v72
	v_lshlrev_b32_e32 v72, 16, v73
	v_add_f32_e32 v77, v104, v77
	v_add_f32_e32 v81, v81, v103
	v_add_f32_e32 v103, v76, v72
	v_and_b32_e32 v72, 0xffff0000, v73
	v_and_b32_e32 v78, 0xffff0000, v78
	v_add_f32_e32 v104, v77, v72
	v_lshlrev_b32_e32 v72, 16, v74
	v_add_f32_e32 v2, v2, v106
	v_add_f32_e32 v78, v105, v78
	v_add_f32_e32 v80, v80, v72
	v_and_b32_e32 v72, 0xffff0000, v74
	v_add_f32_e32 v2, v2, v79
	v_add_f32_e32 v105, v78, v72
	v_lshlrev_b32_e32 v72, 16, v75
	ds_read_b128 v[76:79], v124 offset:4608
	v_add_f32_e32 v81, v81, v72
	v_and_b32_e32 v72, 0xffff0000, v75
	v_add_f32_e32 v101, v101, v72
	ds_read_b128 v[72:75], v124 offset:5136
	s_waitcnt lgkmcnt(1)
	v_lshlrev_b32_e32 v141, 16, v77
	v_lshlrev_b32_e32 v106, 16, v76
	v_and_b32_e32 v107, 0xffff0000, v76
	v_add_f32_e32 v76, v103, v141
	v_and_b32_e32 v103, 0xffff0000, v77
	v_and_b32_e32 v142, 0xffff0000, v78
	v_add_f32_e32 v3, v3, v107
	v_add_f32_e32 v77, v104, v103
	v_lshlrev_b32_e32 v104, 16, v78
	v_add_f32_e32 v78, v105, v142
	v_lshlrev_b32_e32 v105, 16, v79
	v_and_b32_e32 v143, 0xffff0000, v79
	s_waitcnt lgkmcnt(0)
	v_lshlrev_b32_e32 v79, 16, v72
	v_and_b32_e32 v72, 0xffff0000, v72
	v_add_f32_e32 v3, v3, v72
	v_lshlrev_b32_e32 v72, 16, v73
	v_add_f32_e32 v144, v76, v72
	v_and_b32_e32 v72, 0xffff0000, v73
	v_add_f32_e32 v80, v80, v104
	v_add_f32_e32 v145, v77, v72
	v_lshlrev_b32_e32 v72, 16, v74
	v_add_f32_e32 v2, v2, v106
	v_add_f32_e32 v80, v80, v72
	v_and_b32_e32 v72, 0xffff0000, v74
	v_add_f32_e32 v2, v2, v79
	v_add_f32_e32 v146, v78, v72
	ds_read_b128 v[76:79], v124 offset:5664
	v_add_f32_e32 v81, v81, v105
	v_lshlrev_b32_e32 v72, 16, v75
	v_add_f32_e32 v101, v101, v143
	v_add_f32_e32 v81, v81, v72
	v_and_b32_e32 v72, 0xffff0000, v75
	v_add_f32_e32 v101, v101, v72
	ds_read_b128 v[72:75], v124 offset:6192
	s_waitcnt lgkmcnt(1)
	v_lshlrev_b32_e32 v147, 16, v76
	v_and_b32_e32 v76, 0xffff0000, v76
	v_add_f32_e32 v3, v3, v76
	v_lshlrev_b32_e32 v76, 16, v77
	v_add_f32_e32 v76, v144, v76
	v_lshlrev_b32_e32 v144, 16, v78
	v_add_f32_e32 v80, v80, v144
	v_lshlrev_b32_e32 v144, 16, v79
	v_and_b32_e32 v79, 0xffff0000, v79
	v_add_f32_e32 v101, v101, v79
	s_waitcnt lgkmcnt(0)
	v_lshlrev_b32_e32 v79, 16, v72
	v_and_b32_e32 v72, 0xffff0000, v72
	v_and_b32_e32 v77, 0xffff0000, v77
	v_add_f32_e32 v3, v3, v72
	v_lshlrev_b32_e32 v72, 16, v73
	v_add_f32_e32 v77, v145, v77
	v_add_f32_e32 v81, v81, v144
	v_add_f32_e32 v144, v76, v72
	v_and_b32_e32 v72, 0xffff0000, v73
	v_and_b32_e32 v78, 0xffff0000, v78
	v_add_f32_e32 v145, v77, v72
	v_lshlrev_b32_e32 v72, 16, v74
	v_add_f32_e32 v2, v2, v147
	v_add_f32_e32 v78, v146, v78
	v_add_f32_e32 v80, v80, v72
	v_and_b32_e32 v72, 0xffff0000, v74
	v_add_f32_e32 v2, v2, v79
	v_add_f32_e32 v146, v78, v72
	ds_read_b128 v[76:79], v124 offset:6720
	v_lshlrev_b32_e32 v72, 16, v75
	v_add_f32_e32 v81, v81, v72
	v_and_b32_e32 v72, 0xffff0000, v75
	v_add_f32_e32 v101, v101, v72
	ds_read_b128 v[72:75], v124 offset:7248
	s_waitcnt lgkmcnt(1)
	v_lshlrev_b32_e32 v147, 16, v76
	v_and_b32_e32 v76, 0xffff0000, v76
	v_add_f32_e32 v3, v3, v76
	v_lshlrev_b32_e32 v76, 16, v77
	v_add_f32_e32 v76, v144, v76
	v_lshlrev_b32_e32 v144, 16, v78
	v_add_f32_e32 v80, v80, v144
	v_lshlrev_b32_e32 v144, 16, v79
	v_and_b32_e32 v79, 0xffff0000, v79
	v_add_f32_e32 v101, v101, v79
	s_waitcnt lgkmcnt(0)
	v_lshlrev_b32_e32 v79, 16, v72
	v_and_b32_e32 v72, 0xffff0000, v72
	v_and_b32_e32 v77, 0xffff0000, v77
	v_add_f32_e32 v3, v3, v72
	v_lshlrev_b32_e32 v72, 16, v73
	v_add_f32_e32 v77, v145, v77
	v_add_f32_e32 v81, v81, v144
	v_add_f32_e32 v144, v76, v72
	v_and_b32_e32 v72, 0xffff0000, v73
	v_and_b32_e32 v78, 0xffff0000, v78
	v_add_f32_e32 v145, v77, v72
	v_lshlrev_b32_e32 v72, 16, v74
	v_add_f32_e32 v2, v2, v147
	v_add_f32_e32 v78, v146, v78
	v_add_f32_e32 v80, v80, v72
	v_and_b32_e32 v72, 0xffff0000, v74
	v_add_f32_e32 v2, v2, v79
	v_add_f32_e32 v146, v78, v72
	ds_read_b128 v[76:79], v124 offset:7776
	v_lshlrev_b32_e32 v72, 16, v75
	v_add_f32_e32 v81, v81, v72
	v_and_b32_e32 v72, 0xffff0000, v75
	v_add_f32_e32 v101, v101, v72
	ds_read_b128 v[72:75], v124 offset:8304
	s_waitcnt lgkmcnt(1)
	v_lshlrev_b32_e32 v147, 16, v76
	v_and_b32_e32 v76, 0xffff0000, v76
	v_add_f32_e32 v3, v3, v76
	v_lshlrev_b32_e32 v76, 16, v77
	v_add_f32_e32 v76, v144, v76
	v_lshlrev_b32_e32 v144, 16, v78
	v_add_f32_e32 v80, v80, v144
	v_lshlrev_b32_e32 v144, 16, v79
	v_and_b32_e32 v79, 0xffff0000, v79
	v_and_b32_e32 v77, 0xffff0000, v77
	v_add_f32_e32 v79, v101, v79
	s_waitcnt lgkmcnt(0)
	v_lshlrev_b32_e32 v101, 16, v72
	v_and_b32_e32 v72, 0xffff0000, v72
	v_add_f32_e32 v77, v145, v77
	v_add_f32_e32 v3, v3, v72
	v_lshlrev_b32_e32 v72, 16, v73
	v_and_b32_e32 v73, 0xffff0000, v73
	v_add_f32_e32 v73, v77, v73
	v_add_u32_e32 v77, 8, v1
	v_max_i32_e32 v1, 8, v1
	v_min_i32_e32 v77, s14, v77
	v_sub_u32_e32 v1, v77, v1
	v_add_u32_e32 v1, 8, v1
	v_cvt_f32_i32_e32 v1, v1
	v_and_b32_e32 v78, 0xffff0000, v78
	v_add_f32_e32 v78, v146, v78
	v_add_f32_e32 v72, v76, v72
	v_lshlrev_b32_e32 v76, 16, v74
	v_and_b32_e32 v74, 0xffff0000, v74
	v_add_f32_e32 v74, v78, v74
	v_div_scale_f32 v78, s[10:11], v1, v1, 1.0
	v_add_f32_e32 v76, v80, v76
	v_rcp_f32_e32 v80, v78
	v_lshlrev_b32_e32 v77, 16, v75
	v_and_b32_e32 v75, 0xffff0000, v75
	v_add_f32_e32 v75, v79, v75
	v_fma_f32 v79, -v78, v80, 1.0
	v_add_f32_e32 v81, v81, v144
	v_fmac_f32_e32 v80, v79, v80
	v_div_scale_f32 v79, vcc, 1.0, v1, 1.0
	v_add_f32_e32 v2, v2, v147
	v_add_f32_e32 v77, v81, v77
	v_mul_f32_e32 v81, v79, v80
	v_add_f32_e32 v2, v2, v101
	v_fma_f32 v101, -v78, v81, v79
	v_fmac_f32_e32 v81, v101, v80
	v_fma_f32 v78, -v78, v81, v79
	v_div_fmas_f32 v78, v78, v80, v81
	v_div_fixup_f32 v1, v78, v1, 1.0
	v_fma_f32 v73, v1, v73, -v103
	v_fma_f32 v74, v1, v74, -v142
	v_fma_f32 v2, v1, v2, -v106
	v_fma_f32 v3, v1, v3, -v107
	v_fma_f32 v78, v1, v72, -v141
	v_fma_f32 v76, v1, v76, -v104
	v_fma_f32 v77, v1, v77, -v105
	v_fma_f32 v1, v1, v75, -v143
	v_cvt_pk_bf16_f32 v72, v2, v3
	v_cvt_pk_bf16_f32 v73, v78, v73
	v_cvt_pk_bf16_f32 v74, v76, v74
	v_cvt_pk_bf16_f32 v75, v77, v1
	ds_write_b128 v124, v[72:75] offset:45440
	s_waitcnt lgkmcnt(0)
	s_barrier
	ds_read_b128 v[72:75], v140 offset:45056
	ds_read_b128 v[162:165], v140 offset:45120
	s_waitcnt lgkmcnt(1)
	v_mfma_f32_16x16x32_bf16 v[76:79], v[4:7], v[72:75], 0
	ds_read_b128 v[146:149], v140 offset:53504
	v_or_b32_e32 v1, s26, v115
	v_add_u32_e32 v2, s27, v1
	v_mfma_f32_16x16x32_bf16 v[104:107], v[8:11], v[72:75], 0
	v_ashrrev_i32_e32 v3, 31, v2
	v_lshlrev_b64 v[2:3], 10, v[2:3]
	v_lshl_add_u64 v[2:3], v[98:99], 0, v[2:3]
	s_waitcnt lgkmcnt(1)
	v_mfma_f32_16x16x32_bf16 v[76:79], v[20:23], v[162:165], v[76:79]
	v_mfma_f32_16x16x32_bf16 v[104:107], v[24:27], v[162:165], v[104:107]
	v_mfma_f32_16x16x32_bf16 v[142:145], v[12:15], v[72:75], 0
	s_nop 5
	v_mul_f32_e64 v80, v76, v56
	v_mul_f32_e64 v81, v77, v57
	v_cvt_pk_fp8_f32 v76, v80, v81
	v_mfma_f32_16x16x32_bf16 v[72:75], v[16:19], v[72:75], 0
	v_mul_f32_e64 v80, v104, v64
	v_mul_f32_e64 v81, v105, v65
	v_cvt_pk_fp8_f32 v77, v80, v81
	v_mfma_f32_16x16x32_bf16 v[142:145], v[28:31], v[162:165], v[142:145]
	v_mul_f32_e64 v78, v78, v58
	v_mul_f32_e64 v79, v79, v59
	v_cvt_pk_fp8_f32 v76, v78, v79 op_sel:[0,0,1]
	v_mfma_f32_16x16x32_bf16 v[72:75], v[32:35], v[162:165], v[72:75]
	ds_read_b128 v[162:165], v140 offset:53568
	v_pk_mul_f32 v[78:79], v[106:107], v[66:67]
	s_nop 1
	v_pk_mul_f32 v[80:81], v[142:143], v[60:61]
	s_waitcnt lgkmcnt(1)
	v_mfma_f32_16x16x32_bf16 v[150:153], v[4:7], v[146:149], 0
	v_cvt_pk_fp8_f32 v77, v78, v79 op_sel:[0,0,1]
	v_cvt_pk_fp8_f32 v78, v80, v81
	v_mfma_f32_16x16x32_bf16 v[154:157], v[8:11], v[146:149], 0
	v_mul_f32_e64 v72, v72, v68
	v_mul_f32_e64 v73, v73, v69
	v_cvt_pk_fp8_f32 v79, v72, v73
	s_waitcnt lgkmcnt(0)
	v_mfma_f32_16x16x32_bf16 v[150:153], v[20:23], v[162:165], v[150:153]
	v_mul_f32_e64 v72, v144, v62
	v_mul_f32_e64 v73, v145, v63
	v_cvt_pk_fp8_f32 v78, v72, v73 op_sel:[0,0,1]
	v_mfma_f32_16x16x32_bf16 v[154:157], v[24:27], v[162:165], v[154:157]
	v_mul_f32_e64 v72, v74, v70
	v_mul_f32_e64 v73, v75, v71
	s_nop 1
	v_pk_mul_f32 v[74:75], v[150:151], v[56:57]
	v_cvt_pk_fp8_f32 v79, v72, v73 op_sel:[0,0,1]
	v_mfma_f32_16x16x32_bf16 v[158:161], v[12:15], v[146:149], 0
	v_cvt_pk_fp8_f32 v72, v74, v75
	v_pk_mul_f32 v[74:75], v[154:155], v[64:65]
	v_mfma_f32_16x16x32_bf16 v[146:149], v[16:19], v[146:149], 0
	v_cvt_pk_fp8_f32 v73, v74, v75
	v_permlane32_swap_b32_e32 v76, v78
	v_mfma_f32_16x16x32_bf16 v[158:161], v[28:31], v[162:165], v[158:161]
	v_permlane32_swap_b32_e32 v77, v79
	v_pk_mul_f32 v[74:75], v[152:153], v[58:59]
	v_mfma_f32_16x16x32_bf16 v[146:149], v[32:35], v[162:165], v[146:149]
	v_permlane16_swap_b32_e32 v76, v77
	v_permlane16_swap_b32_e32 v78, v79
	v_cvt_pk_fp8_f32 v72, v74, v75 op_sel:[0,0,1]
	v_pk_mul_f32 v[74:75], v[156:157], v[66:67]
	global_store_dwordx4 v[2:3], v[76:79], off offset:512
	v_cvt_pk_fp8_f32 v73, v74, v75 op_sel:[0,0,1]
	v_pk_mul_f32 v[76:77], v[158:159], v[60:61]
	v_cvt_pk_fp8_f32 v74, v76, v77
	v_pk_mul_f32 v[76:77], v[146:147], v[68:69]
	v_add_co_u32_e32 v2, vcc, 0x4000, v2
	v_cvt_pk_fp8_f32 v75, v76, v77
	v_pk_mul_f32 v[76:77], v[160:161], v[62:63]
	v_addc_co_u32_e32 v3, vcc, 0, v3, vcc
	v_cvt_pk_fp8_f32 v74, v76, v77 op_sel:[0,0,1]
	v_pk_mul_f32 v[76:77], v[148:149], v[70:71]
	s_andn2_b64 vcc, exec, s[20:21]
	v_cvt_pk_fp8_f32 v75, v76, v77 op_sel:[0,0,1]
	v_permlane32_swap_b32_e32 v72, v74
	s_nop 0
	v_permlane32_swap_b32_e32 v73, v75
	s_nop 1
	v_permlane16_swap_b32_e32 v72, v73
	v_permlane16_swap_b32_e32 v74, v75
	global_store_dwordx4 v[2:3], v[72:75], off offset:512
	s_cbranch_vccnz .LBB0_578
	s_waitcnt vmcnt(0)
	s_barrier
	s_and_saveexec_b64 s[94:95], s[0:1]
	s_cbranch_execz .LBB0_577
	s_mov_b64 s[10:11], exec
	v_mbcnt_lo_u32_b32 v1, s10, 0
	buffer_wbl2 sc1
	s_waitcnt vmcnt(0)
	s_waitcnt vmcnt(0)
	v_mbcnt_hi_u32_b32 v1, s11, v1
	v_cmp_eq_u32_e32 vcc, 0, v1
	s_and_b64 s[14:15], exec, vcc
	s_mov_b64 exec, s[14:15]
	s_cbranch_execz .LBB0_577
	s_bcnt1_i32_b64 s10, s[10:11]
	v_mov_b32_e32 v1, s10
	global_atomic_add v0, v1, s[84:85]
	s_branch .LBB0_577
